# merge GEMM (P5) k-loop also gets the static priority raise for waves 4-7 with its per-segment flips deleted
# speedup vs baseline: 1.0005x; 1.0005x over previous
.LBB0_1345:
	s_ashr_i32 s13, s12, 31
	s_lshl_b64 s[14:15], s[12:13], 21
	v_readlane_b32 s16, v254, 40
	v_readlane_b32 s17, v254, 41
	s_add_u32 s14, s16, s14
	s_addc_u32 s15, s17, s15
	s_and_b64 s[16:17], s[2:3], exec
	s_cselect_b32 s13, s15, s19
	s_cselect_b32 s43, s14, s18
	s_ashr_i32 s11, s10, 31
	s_lshl_b64 s[16:17], s[10:11], 21
	v_readlane_b32 s24, v254, 44
	v_readlane_b32 s25, v254, 45
	s_add_u32 s16, s24, s16
	s_addc_u32 s17, s25, s17
	s_and_b64 s[24:25], s[2:3], exec
	s_cselect_b32 s11, s17, s23
	s_cselect_b32 s44, s16, s22
	s_lshl_b32 s21, s21, 9
	s_lshl_b32 s20, s20, 21
	s_add_i32 s20, s20, s21
	v_mov_b32_e32 v4, v2
	v_mov_b32_e32 v5, v2
	s_add_u32 s45, s22, 0x100
	v_mov_b32_e32 v3, v2
	v_mov_b64_e32 v[8:9], v[4:5]
	v_mov_b64_e32 v[12:13], v[4:5]
	v_mov_b64_e32 v[24:25], v[4:5]
	v_mov_b64_e32 v[28:29], v[4:5]
	v_mov_b64_e32 v[40:41], v[4:5]
	v_mov_b64_e32 v[44:45], v[4:5]
	v_mov_b64_e32 v[56:57], v[4:5]
	v_mov_b64_e32 v[60:61], v[4:5]
	v_mov_b64_e32 v[16:17], v[4:5]
	v_mov_b64_e32 v[20:21], v[4:5]
	v_mov_b64_e32 v[32:33], v[4:5]
	v_mov_b64_e32 v[36:37], v[4:5]
	v_mov_b64_e32 v[48:49], v[4:5]
	v_mov_b64_e32 v[52:53], v[4:5]
	v_mov_b64_e32 v[64:65], v[4:5]
	v_mov_b64_e32 v[68:69], v[4:5]
	v_mov_b64_e32 v[72:73], v[4:5]
	v_mov_b64_e32 v[76:77], v[4:5]
	v_mov_b64_e32 v[88:89], v[4:5]
	v_mov_b64_e32 v[92:93], v[4:5]
	v_mov_b64_e32 v[104:105], v[4:5]
	v_mov_b64_e32 v[108:109], v[4:5]
	v_mov_b64_e32 v[120:121], v[4:5]
	v_mov_b64_e32 v[124:125], v[4:5]
	v_mov_b64_e32 v[80:81], v[4:5]
	v_mov_b64_e32 v[84:85], v[4:5]
	v_mov_b64_e32 v[96:97], v[4:5]
	v_mov_b64_e32 v[100:101], v[4:5]
	v_mov_b64_e32 v[112:113], v[4:5]
	v_mov_b64_e32 v[116:117], v[4:5]
	v_mov_b64_e32 v[128:129], v[4:5]
	v_mov_b64_e32 v[132:133], v[4:5]
	v_add_u32_e32 v181, s20, v167
	v_lshl_add_u64 v[176:177], s[18:19], 0, v[168:169]
	v_lshl_add_u64 v[178:179], s[18:19], 0, v[170:171]
	s_addc_u32 s46, s23, 0
	s_mov_b32 s47, -2
	s_mov_b64 s[20:21], 0
	v_mov_b64_e32 v[6:7], v[2:3]
	v_mov_b64_e32 v[10:11], v[2:3]
	v_mov_b64_e32 v[22:23], v[2:3]
	v_mov_b64_e32 v[26:27], v[2:3]
	v_mov_b64_e32 v[38:39], v[2:3]
	v_mov_b64_e32 v[42:43], v[2:3]
	v_mov_b64_e32 v[54:55], v[2:3]
	v_mov_b64_e32 v[58:59], v[2:3]
	v_mov_b64_e32 v[14:15], v[2:3]
	v_mov_b64_e32 v[18:19], v[2:3]
	v_mov_b64_e32 v[30:31], v[2:3]
	v_mov_b64_e32 v[34:35], v[2:3]
	v_mov_b64_e32 v[46:47], v[2:3]
	v_mov_b64_e32 v[50:51], v[2:3]
	v_mov_b64_e32 v[62:63], v[2:3]
	v_mov_b64_e32 v[66:67], v[2:3]
	v_mov_b64_e32 v[70:71], v[2:3]
	v_mov_b64_e32 v[74:75], v[2:3]
	v_mov_b64_e32 v[86:87], v[2:3]
	v_mov_b64_e32 v[90:91], v[2:3]
	v_mov_b64_e32 v[102:103], v[2:3]
	v_mov_b64_e32 v[106:107], v[2:3]
	v_mov_b64_e32 v[118:119], v[2:3]
	v_mov_b64_e32 v[122:123], v[2:3]
	v_mov_b64_e32 v[78:79], v[2:3]
	v_mov_b64_e32 v[82:83], v[2:3]
	v_mov_b64_e32 v[94:95], v[2:3]
	v_mov_b64_e32 v[98:99], v[2:3]
	v_mov_b64_e32 v[110:111], v[2:3]
	v_mov_b64_e32 v[114:115], v[2:3]
	v_mov_b64_e32 v[126:127], v[2:3]
	v_mov_b64_e32 v[130:131], v[2:3]
	v_readfirstlane_b32 s22, v0
	s_nop 3
	s_lshr_b32 s22, s22, 6
	s_cmp_ge_u32 s22, 4
	s_cbranch_scc0 .Lprio_P5
	s_setprio 1
.Lprio_P5:
	s_branch .LBB0_1347
.LBB0_1346:
	v_add_u32_e32 v3, s37, v1
	ds_read_b128 v[134:137], v3
	ds_read_b128 v[138:141], v3 offset:1024
	ds_read_b128 v[142:145], v3 offset:2048
	ds_read_b128 v[146:149], v3 offset:3072
	v_add_u32_e32 v3, s42, v1
	s_add_u32 s22, s18, s20
	ds_read_b128 v[150:153], v3
	ds_read_b128 v[154:157], v3 offset:1024
	ds_read_b128 v[182:185], v3 offset:2048
	ds_read_b128 v[186:189], v3 offset:3072
	s_addc_u32 s23, s19, s21
	s_add_u32 s22, s22, 0x100
	s_addc_u32 s23, s23, 0
	s_add_u32 s38, s45, s20
	s_addc_u32 s39, s46, s21
	s_cmpk_eq_i32 s20, 0x1f00
	s_cselect_b32 s25, s13, s23
	s_cselect_b32 s24, s43, s22
	s_cselect_b32 s23, s11, s39
	s_cselect_b32 s22, s44, s38
	v_lshl_add_u64 v[4:5], v[176:177], 0, s[20:21]
	s_add_i32 m0, s28, 0xc000
	ds_read_b128 v[190:193], v180
	ds_read_b128 v[194:197], v180 offset:1024
	ds_read_b128 v[198:201], v180 offset:2048
	ds_read_b128 v[202:205], v180 offset:3072
	ds_read_b128 v[206:209], v180 offset:4096
	ds_read_b128 v[210:213], v180 offset:5120
	ds_read_b128 v[214:217], v180 offset:6144
	ds_read_b128 v[218:221], v180 offset:7168
	global_load_lds_dwordx4 v[4:5], off
	v_lshl_add_u64 v[4:5], v[178:179], 0, s[20:21]
	s_add_i32 m0, s28, 0xe000
	s_nop 0
	global_load_lds_dwordx4 v[4:5], off
	s_waitcnt vmcnt(8)
	s_waitcnt lgkmcnt(0)
	s_barrier
	s_waitcnt lgkmcnt(0)
	v_mfma_f32_16x16x32_bf16 v[130:133], v[134:137], v[190:193], v[130:133]
	v_mfma_f32_16x16x32_bf16 v[126:129], v[142:145], v[190:193], v[126:129]
	v_mfma_f32_16x16x32_bf16 v[114:117], v[134:137], v[198:201], v[114:117]
	v_mfma_f32_16x16x32_bf16 v[110:113], v[142:145], v[198:201], v[110:113]
	v_mfma_f32_16x16x32_bf16 v[98:101], v[134:137], v[206:209], v[98:101]
	v_mfma_f32_16x16x32_bf16 v[94:97], v[142:145], v[206:209], v[94:97]
	v_mfma_f32_16x16x32_bf16 v[82:85], v[134:137], v[214:217], v[82:85]
	v_mfma_f32_16x16x32_bf16 v[78:81], v[142:145], v[214:217], v[78:81]
	v_mfma_f32_16x16x32_bf16 v[130:133], v[138:141], v[194:197], v[130:133]
	v_mfma_f32_16x16x32_bf16 v[126:129], v[146:149], v[194:197], v[126:129]
	v_mfma_f32_16x16x32_bf16 v[114:117], v[138:141], v[202:205], v[114:117]
	v_mfma_f32_16x16x32_bf16 v[110:113], v[146:149], v[202:205], v[110:113]
	v_mfma_f32_16x16x32_bf16 v[98:101], v[138:141], v[210:213], v[98:101]
	v_mfma_f32_16x16x32_bf16 v[94:97], v[146:149], v[210:213], v[94:97]
	v_mfma_f32_16x16x32_bf16 v[82:85], v[138:141], v[218:221], v[82:85]
	v_mfma_f32_16x16x32_bf16 v[78:81], v[146:149], v[218:221], v[78:81]
	v_mfma_f32_16x16x32_bf16 v[122:125], v[150:153], v[190:193], v[122:125]
	v_mfma_f32_16x16x32_bf16 v[118:121], v[182:185], v[190:193], v[118:121]
	v_mfma_f32_16x16x32_bf16 v[106:109], v[150:153], v[198:201], v[106:109]
	v_mfma_f32_16x16x32_bf16 v[102:105], v[182:185], v[198:201], v[102:105]
	v_mfma_f32_16x16x32_bf16 v[90:93], v[150:153], v[206:209], v[90:93]
	v_mfma_f32_16x16x32_bf16 v[86:89], v[182:185], v[206:209], v[86:89]
	v_mfma_f32_16x16x32_bf16 v[74:77], v[150:153], v[214:217], v[74:77]
	v_mfma_f32_16x16x32_bf16 v[70:73], v[182:185], v[214:217], v[70:73]
	v_mfma_f32_16x16x32_bf16 v[122:125], v[154:157], v[194:197], v[122:125]
	v_mfma_f32_16x16x32_bf16 v[118:121], v[186:189], v[194:197], v[118:121]
	v_mfma_f32_16x16x32_bf16 v[106:109], v[154:157], v[202:205], v[106:109]
	v_mfma_f32_16x16x32_bf16 v[102:105], v[186:189], v[202:205], v[102:105]
	v_mfma_f32_16x16x32_bf16 v[90:93], v[154:157], v[210:213], v[90:93]
	v_mfma_f32_16x16x32_bf16 v[86:89], v[186:189], v[210:213], v[86:89]
	v_mfma_f32_16x16x32_bf16 v[74:77], v[154:157], v[218:221], v[74:77]
	v_mfma_f32_16x16x32_bf16 v[70:73], v[186:189], v[218:221], v[70:73]
	s_barrier
	s_add_i32 s38, s37, s27
	v_lshl_add_u64 v[222:223], s[22:23], 0, v[160:161]
	s_mov_b32 m0, s38
	ds_read_b128 v[190:193], v180 offset:16384
	ds_read_b128 v[194:197], v180 offset:17408
	ds_read_b128 v[198:201], v180 offset:18432
	ds_read_b128 v[202:205], v180 offset:19456
	ds_read_b128 v[206:209], v180 offset:20480
	ds_read_b128 v[210:213], v180 offset:21504
	ds_read_b128 v[214:217], v180 offset:22528
	ds_read_b128 v[218:221], v180 offset:23552
	global_load_lds_dwordx4 v[222:223], off
	s_add_i32 m0, s38, 0x2000
	s_add_u32 s38, s22, 0x100000
	v_lshl_add_u64 v[224:225], s[22:23], 0, v[164:165]
	s_addc_u32 s39, s23, 0
	s_add_i32 s50, s42, s27
	global_load_lds_dwordx4 v[224:225], off
	v_lshl_add_u64 v[4:5], s[38:39], 0, v[160:161]
	s_mov_b32 m0, s50
	v_lshl_add_u64 v[226:227], s[24:25], 0, v[158:159]
	global_load_lds_dwordx4 v[4:5], off
	v_lshl_add_u64 v[4:5], s[38:39], 0, v[164:165]
	s_add_i32 m0, s50, 0x2000
	v_lshl_add_u64 v[228:229], s[24:25], 0, v[162:163]
	global_load_lds_dwordx4 v[4:5], off
	s_mov_b32 m0, s28
	s_nop 0
	global_load_lds_dwordx4 v[226:227], off
	s_mov_b32 m0, s29
	s_nop 0
	global_load_lds_dwordx4 v[228:229], off
	s_waitcnt vmcnt(8)
	s_waitcnt lgkmcnt(0)
	s_barrier
	s_waitcnt lgkmcnt(0)
	v_mfma_f32_16x16x32_bf16 v[66:69], v[134:137], v[190:193], v[66:69]
	v_mfma_f32_16x16x32_bf16 v[62:65], v[142:145], v[190:193], v[62:65]
	v_mfma_f32_16x16x32_bf16 v[50:53], v[134:137], v[198:201], v[50:53]
	v_mfma_f32_16x16x32_bf16 v[46:49], v[142:145], v[198:201], v[46:49]
	v_mfma_f32_16x16x32_bf16 v[34:37], v[134:137], v[206:209], v[34:37]
	v_mfma_f32_16x16x32_bf16 v[30:33], v[142:145], v[206:209], v[30:33]
	v_mfma_f32_16x16x32_bf16 v[18:21], v[134:137], v[214:217], v[18:21]
	v_mfma_f32_16x16x32_bf16 v[14:17], v[142:145], v[214:217], v[14:17]
	v_mfma_f32_16x16x32_bf16 v[66:69], v[138:141], v[194:197], v[66:69]
	v_mfma_f32_16x16x32_bf16 v[62:65], v[146:149], v[194:197], v[62:65]
	v_mfma_f32_16x16x32_bf16 v[50:53], v[138:141], v[202:205], v[50:53]
	v_mfma_f32_16x16x32_bf16 v[46:49], v[146:149], v[202:205], v[46:49]
	v_mfma_f32_16x16x32_bf16 v[34:37], v[138:141], v[210:213], v[34:37]
	v_mfma_f32_16x16x32_bf16 v[30:33], v[146:149], v[210:213], v[30:33]
	v_mfma_f32_16x16x32_bf16 v[18:21], v[138:141], v[218:221], v[18:21]
	v_mfma_f32_16x16x32_bf16 v[14:17], v[146:149], v[218:221], v[14:17]
	v_mfma_f32_16x16x32_bf16 v[58:61], v[150:153], v[190:193], v[58:61]
	v_mfma_f32_16x16x32_bf16 v[54:57], v[182:185], v[190:193], v[54:57]
	v_mfma_f32_16x16x32_bf16 v[42:45], v[150:153], v[198:201], v[42:45]
	v_mfma_f32_16x16x32_bf16 v[38:41], v[182:185], v[198:201], v[38:41]
	v_mfma_f32_16x16x32_bf16 v[26:29], v[150:153], v[206:209], v[26:29]
	v_mfma_f32_16x16x32_bf16 v[22:25], v[182:185], v[206:209], v[22:25]
	v_mfma_f32_16x16x32_bf16 v[10:13], v[150:153], v[214:217], v[10:13]
	v_mfma_f32_16x16x32_bf16 v[4:7], v[182:185], v[214:217], v[6:9]
	v_mfma_f32_16x16x32_bf16 v[58:61], v[154:157], v[194:197], v[58:61]
	v_mfma_f32_16x16x32_bf16 v[54:57], v[186:189], v[194:197], v[54:57]
	v_mfma_f32_16x16x32_bf16 v[42:45], v[154:157], v[202:205], v[42:45]
	v_mfma_f32_16x16x32_bf16 v[38:41], v[186:189], v[202:205], v[38:41]
	v_mfma_f32_16x16x32_bf16 v[26:29], v[154:157], v[210:213], v[26:29]
	v_mfma_f32_16x16x32_bf16 v[22:25], v[186:189], v[210:213], v[22:25]
	v_mfma_f32_16x16x32_bf16 v[10:13], v[154:157], v[218:221], v[10:13]
	v_mfma_f32_16x16x32_bf16 v[4:7], v[186:189], v[218:221], v[4:7]
	s_barrier
	s_add_i32 s38, 0, 0x18000
	v_add_u32_e32 v3, s38, v1
	s_add_i32 s39, 0, 0x1c000
	ds_read_b128 v[134:137], v3
	ds_read_b128 v[138:141], v3 offset:1024
	ds_read_b128 v[142:145], v3 offset:2048
	ds_read_b128 v[146:149], v3 offset:3072
	v_add_u32_e32 v3, s39, v1
	ds_read_b128 v[150:153], v3
	ds_read_b128 v[154:157], v3 offset:1024
	ds_read_b128 v[182:185], v3 offset:2048
	ds_read_b128 v[186:189], v3 offset:3072
	s_add_u32 s24, s24, 0x100000
	s_addc_u32 s25, s25, 0
	s_mov_b32 m0, s30
	v_lshl_add_u64 v[8:9], s[24:25], 0, v[158:159]
	ds_read_b128 v[190:193], v180 offset:32768
	ds_read_b128 v[194:197], v180 offset:33792
	ds_read_b128 v[198:201], v180 offset:34816
	ds_read_b128 v[202:205], v180 offset:35840
	ds_read_b128 v[206:209], v180 offset:36864
	ds_read_b128 v[210:213], v180 offset:37888
	ds_read_b128 v[214:217], v180 offset:38912
	ds_read_b128 v[218:221], v180 offset:39936
	global_load_lds_dwordx4 v[8:9], off
	v_lshl_add_u64 v[8:9], s[24:25], 0, v[162:163]
	s_mov_b32 m0, s31
	s_nop 0
	global_load_lds_dwordx4 v[8:9], off
	s_waitcnt vmcnt(8)
	s_waitcnt lgkmcnt(0)
	s_barrier
	s_waitcnt lgkmcnt(0)
	v_mfma_f32_16x16x32_bf16 v[130:133], v[134:137], v[190:193], v[130:133]
	v_mfma_f32_16x16x32_bf16 v[126:129], v[142:145], v[190:193], v[126:129]
	v_mfma_f32_16x16x32_bf16 v[114:117], v[134:137], v[198:201], v[114:117]
	v_mfma_f32_16x16x32_bf16 v[110:113], v[142:145], v[198:201], v[110:113]
	v_mfma_f32_16x16x32_bf16 v[98:101], v[134:137], v[206:209], v[98:101]
	v_mfma_f32_16x16x32_bf16 v[94:97], v[142:145], v[206:209], v[94:97]
	v_mfma_f32_16x16x32_bf16 v[82:85], v[134:137], v[214:217], v[82:85]
	v_mfma_f32_16x16x32_bf16 v[78:81], v[142:145], v[214:217], v[78:81]
	v_mfma_f32_16x16x32_bf16 v[130:133], v[138:141], v[194:197], v[130:133]
	v_mfma_f32_16x16x32_bf16 v[126:129], v[146:149], v[194:197], v[126:129]
	v_mfma_f32_16x16x32_bf16 v[114:117], v[138:141], v[202:205], v[114:117]
	v_mfma_f32_16x16x32_bf16 v[110:113], v[146:149], v[202:205], v[110:113]
	v_mfma_f32_16x16x32_bf16 v[98:101], v[138:141], v[210:213], v[98:101]
	v_mfma_f32_16x16x32_bf16 v[94:97], v[146:149], v[210:213], v[94:97]
	v_mfma_f32_16x16x32_bf16 v[82:85], v[138:141], v[218:221], v[82:85]
	v_mfma_f32_16x16x32_bf16 v[78:81], v[146:149], v[218:221], v[78:81]
	v_mfma_f32_16x16x32_bf16 v[122:125], v[150:153], v[190:193], v[122:125]
	v_mfma_f32_16x16x32_bf16 v[118:121], v[182:185], v[190:193], v[118:121]
	v_mfma_f32_16x16x32_bf16 v[106:109], v[150:153], v[198:201], v[106:109]
	v_mfma_f32_16x16x32_bf16 v[102:105], v[182:185], v[198:201], v[102:105]
	v_mfma_f32_16x16x32_bf16 v[90:93], v[150:153], v[206:209], v[90:93]
	v_mfma_f32_16x16x32_bf16 v[86:89], v[182:185], v[206:209], v[86:89]
	v_mfma_f32_16x16x32_bf16 v[74:77], v[150:153], v[214:217], v[74:77]
	v_mfma_f32_16x16x32_bf16 v[70:73], v[182:185], v[214:217], v[70:73]
	v_mfma_f32_16x16x32_bf16 v[122:125], v[154:157], v[194:197], v[122:125]
	v_mfma_f32_16x16x32_bf16 v[118:121], v[186:189], v[194:197], v[118:121]
	v_mfma_f32_16x16x32_bf16 v[106:109], v[154:157], v[202:205], v[106:109]
	v_mfma_f32_16x16x32_bf16 v[102:105], v[186:189], v[202:205], v[102:105]
	v_mfma_f32_16x16x32_bf16 v[90:93], v[154:157], v[210:213], v[90:93]
	v_mfma_f32_16x16x32_bf16 v[86:89], v[186:189], v[210:213], v[86:89]
	v_mfma_f32_16x16x32_bf16 v[74:77], v[154:157], v[218:221], v[74:77]
	v_mfma_f32_16x16x32_bf16 v[70:73], v[186:189], v[218:221], v[70:73]
	s_barrier
	s_add_i32 s24, s38, s27
	v_lshl_add_u64 v[8:9], v[222:223], 0, s[6:7]
	s_mov_b32 m0, s24
	ds_read_b128 v[190:193], v180 offset:49152
	ds_read_b128 v[194:197], v180 offset:50176
	ds_read_b128 v[198:201], v180 offset:51200
	ds_read_b128 v[202:205], v180 offset:52224
	ds_read_b128 v[206:209], v180 offset:53248
	ds_read_b128 v[210:213], v180 offset:54272
	ds_read_b128 v[214:217], v180 offset:55296
	ds_read_b128 v[218:221], v180 offset:56320
	global_load_lds_dwordx4 v[8:9], off
	s_add_i32 m0, s24, 0x2000
	s_add_u32 s22, s22, 0x100080
	v_lshl_add_u64 v[8:9], v[224:225], 0, s[6:7]
	s_addc_u32 s23, s23, 0
	s_add_i32 s24, s39, s27
	global_load_lds_dwordx4 v[8:9], off
	v_lshl_add_u64 v[8:9], s[22:23], 0, v[160:161]
	s_mov_b32 m0, s24
	s_nop 0
	global_load_lds_dwordx4 v[8:9], off
	v_lshl_add_u64 v[8:9], s[22:23], 0, v[164:165]
	s_add_i32 m0, s24, 0x2000
	s_nop 0
	global_load_lds_dwordx4 v[8:9], off
	v_lshl_add_u64 v[8:9], v[226:227], 0, s[6:7]
	s_mov_b32 m0, s34
	s_nop 0
	global_load_lds_dwordx4 v[8:9], off
	v_lshl_add_u64 v[8:9], v[228:229], 0, s[6:7]
	s_mov_b32 m0, s35
	s_nop 0
	global_load_lds_dwordx4 v[8:9], off
	s_waitcnt vmcnt(8)
	s_waitcnt lgkmcnt(0)
	s_barrier
	s_waitcnt lgkmcnt(0)
	v_mfma_f32_16x16x32_bf16 v[66:69], v[134:137], v[190:193], v[66:69]
	v_mfma_f32_16x16x32_bf16 v[62:65], v[142:145], v[190:193], v[62:65]
	v_mfma_f32_16x16x32_bf16 v[50:53], v[134:137], v[198:201], v[50:53]
	v_mfma_f32_16x16x32_bf16 v[46:49], v[142:145], v[198:201], v[46:49]
	v_mfma_f32_16x16x32_bf16 v[34:37], v[134:137], v[206:209], v[34:37]
	v_mfma_f32_16x16x32_bf16 v[30:33], v[142:145], v[206:209], v[30:33]
	v_mfma_f32_16x16x32_bf16 v[18:21], v[134:137], v[214:217], v[18:21]
	v_mfma_f32_16x16x32_bf16 v[14:17], v[142:145], v[214:217], v[14:17]
	v_mfma_f32_16x16x32_bf16 v[66:69], v[138:141], v[194:197], v[66:69]
	v_mfma_f32_16x16x32_bf16 v[62:65], v[146:149], v[194:197], v[62:65]
	v_mfma_f32_16x16x32_bf16 v[50:53], v[138:141], v[202:205], v[50:53]
	v_mfma_f32_16x16x32_bf16 v[46:49], v[146:149], v[202:205], v[46:49]
	v_mfma_f32_16x16x32_bf16 v[34:37], v[138:141], v[210:213], v[34:37]
	v_mfma_f32_16x16x32_bf16 v[30:33], v[146:149], v[210:213], v[30:33]
	v_mfma_f32_16x16x32_bf16 v[18:21], v[138:141], v[218:221], v[18:21]
	v_mfma_f32_16x16x32_bf16 v[14:17], v[146:149], v[218:221], v[14:17]
	v_mfma_f32_16x16x32_bf16 v[58:61], v[150:153], v[190:193], v[58:61]
	v_mfma_f32_16x16x32_bf16 v[54:57], v[182:185], v[190:193], v[54:57]
	v_mfma_f32_16x16x32_bf16 v[42:45], v[150:153], v[198:201], v[42:45]
	v_mfma_f32_16x16x32_bf16 v[38:41], v[182:185], v[198:201], v[38:41]
	v_mfma_f32_16x16x32_bf16 v[26:29], v[150:153], v[206:209], v[26:29]
	v_mfma_f32_16x16x32_bf16 v[22:25], v[182:185], v[206:209], v[22:25]
	v_mfma_f32_16x16x32_bf16 v[8:11], v[150:153], v[214:217], v[10:13]
	v_mfma_f32_16x16x32_bf16 v[4:7], v[182:185], v[214:217], v[4:7]
	v_mfma_f32_16x16x32_bf16 v[58:61], v[154:157], v[194:197], v[58:61]
	v_mfma_f32_16x16x32_bf16 v[54:57], v[186:189], v[194:197], v[54:57]
	v_mfma_f32_16x16x32_bf16 v[42:45], v[154:157], v[202:205], v[42:45]
	v_mfma_f32_16x16x32_bf16 v[38:41], v[186:189], v[202:205], v[38:41]
	v_mfma_f32_16x16x32_bf16 v[26:29], v[154:157], v[210:213], v[26:29]
	v_mfma_f32_16x16x32_bf16 v[22:25], v[186:189], v[210:213], v[22:25]
	v_mfma_f32_16x16x32_bf16 v[10:13], v[154:157], v[218:221], v[8:11]
	v_mfma_f32_16x16x32_bf16 v[6:9], v[186:189], v[218:221], v[4:7]
	s_barrier
	s_add_i32 s47, s47, 2
	s_add_u32 s20, s20, 0x100
	s_addc_u32 s21, s21, 0
	s_cmp_gt_u32 s47, 61
	s_cbranch_scc1 .LBB0_1349

.LBB0_1349:
	s_setprio 0
	s_and_b64 vcc, exec, s[8:9]
	s_cbranch_vccz .LBB0_1351
	s_barrier
